# attention boundary key tiles: the 16 exec-masked, serialized LDS bias reads replaced by 8 unconditional ds_read2 + one wait + fmac + cndmask mask-select (same values, -1e30 for masked keys)
# speedup vs baseline: 1.0116x; 1.0116x over previous
; #define LAS __attribute__((address_space(3)))
; DI float other_half(float x, int h) { const u32x2 r = __builtin_amdgcn_permlane32_swap(__builtin_bit_cast(unsigned, x), __builtin_bit_cast(unsigned, x), false, false); return __builtin_bit_cast(float, h ? r.x : r.y); }
; DI int crow(int reg, int h) { return (reg & 3) + 8 * (reg >> 2) + 4 * h; }
; DI void phase_attn(const Frame& F, int j) {
;     ...
;                 if (kt > sub && kt < sub + 8 && qb > 0 && qb < 31) {
;                     const LAS float* bp = bT + hh * 260 + 32 * kt - 32 * sub - r + 4 * h;
; #pragma unroll
;                     for (int i = 0; i < 16; ++i) { const float sc = x[i] * (0.125f * 1.44269504f) + bp[(i & 3) + 8 * (i >> 2)]; x[i] = sc; mt = fmaxf(mt, sc); }
;                 } else {
; #pragma unroll
;                 for (int i = 0; i < 16; ++i) { const int kl = 32 * kt + crow(i, h); const int rel = kl - 128 - qrel; const int kp = q0 - 128 + kl;
;                     const bool ok = rel >= -128 && rel <= 128 && kp >= 0 && kp < SEQ;
;                     const int bi = rel < -128 ? 0 : (rel > 128 ? 256 : rel + 128);
;                     const float sc = ok ? x[i] * (0.125f * 1.44269504f) + bT[hh * 260 + bi] : -1e30f; x[i] = sc; mt = fmaxf(mt, sc); }
;                 }
;                 mt = fmaxf(mt, other_half(mt, h));
.LBB0_358:
	s_and_b64 vcc, exec, s[4:5]
	s_cbranch_vccz .LBB0_392
	v_add_u32_e32 v149, s87, v115
	s_add_i32 s2, s8, s87
	s_cmpk_lt_u32 s2, 0x1000
	s_cselect_b32 s2, s33, 0
	v_add_u32_e32 v148, 0, v147
	v_add_u32_e32 v96, 0x19c80, v148
	ds_read2_b32 v[96:97], v96 offset1:1
	v_add_u32_e32 v98, 0x19c88, v148
	ds_read2_b32 v[98:99], v98 offset1:1
	v_add_u32_e32 v100, 0x19ca0, v148
	ds_read2_b32 v[100:101], v100 offset1:1
	v_add_u32_e32 v102, 0x19ca8, v148
	ds_read2_b32 v[102:103], v102 offset1:1
	v_add_u32_e32 v106, 0x19cc0, v148
	ds_read2_b32 v[106:107], v106 offset1:1
	v_add_u32_e32 v104, 0x19cc8, v148
	ds_read2_b32 v[104:105], v104 offset1:1
	v_add_u32_e32 v108, 0x19ce0, v148
	ds_read2_b32 v[108:109], v108 offset1:1
	v_add_u32_e32 v110, 0x19ce8, v148
	ds_read2_b32 v[110:111], v110 offset1:1
	s_waitcnt lgkmcnt(0)
	v_fmac_f32_e32 v96, 0x3e38aa3b, v32
	v_fmac_f32_e32 v97, 0x3e38aa3b, v33
	v_fmac_f32_e32 v98, 0x3e38aa3b, v34
	v_fmac_f32_e32 v99, 0x3e38aa3b, v35
	v_fmac_f32_e32 v100, 0x3e38aa3b, v36
	v_fmac_f32_e32 v101, 0x3e38aa3b, v37
	v_fmac_f32_e32 v102, 0x3e38aa3b, v38
	v_fmac_f32_e32 v103, 0x3e38aa3b, v39
	v_fmac_f32_e32 v106, 0x3e38aa3b, v40
	v_fmac_f32_e32 v107, 0x3e38aa3b, v41
	v_fmac_f32_e32 v104, 0x3e38aa3b, v42
	v_fmac_f32_e32 v105, 0x3e38aa3b, v43
	v_fmac_f32_e32 v108, 0x3e38aa3b, v44
	v_fmac_f32_e32 v109, 0x3e38aa3b, v45
	v_fmac_f32_e32 v110, 0x3e38aa3b, v46
	v_fmac_f32_e32 v111, 0x3e38aa3b, v47
	v_mov_b32_e32 v33, 0xf149f2ca
	v_add_u32_e32 v34, 32, v149
	v_add_u32_e32 v35, 33, v149
	v_add_u32_e32 v36, 34, v149
	v_add_u32_e32 v37, 35, v149
	v_cmp_gt_u32_e32 vcc, s2, v34
	v_cmp_gt_u32_e64 s[4:5], s2, v35
	v_cmp_gt_u32_e64 s[6:7], s2, v36
	v_cmp_gt_u32_e64 s[12:13], s2, v37
	v_cndmask_b32_e32 v96, v33, v96, vcc
	v_cndmask_b32_e64 v97, v33, v97, s[4:5]
	v_cndmask_b32_e64 v98, v33, v98, s[6:7]
	v_cndmask_b32_e64 v99, v33, v99, s[12:13]
	v_add_u32_e32 v34, 40, v149
	v_add_u32_e32 v35, 41, v149
	v_add_u32_e32 v36, 42, v149
	v_add_u32_e32 v37, 43, v149
	v_cmp_gt_u32_e32 vcc, s2, v34
	v_cmp_gt_u32_e64 s[4:5], s2, v35
	v_cmp_gt_u32_e64 s[6:7], s2, v36
	v_cmp_gt_u32_e64 s[12:13], s2, v37
	v_cndmask_b32_e32 v100, v33, v100, vcc
	v_cndmask_b32_e64 v101, v33, v101, s[4:5]
	v_cndmask_b32_e64 v102, v33, v102, s[6:7]
	v_cndmask_b32_e64 v103, v33, v103, s[12:13]
	v_add_u32_e32 v34, 48, v149
	v_add_u32_e32 v35, 49, v149
	v_add_u32_e32 v36, 50, v149
	v_add_u32_e32 v37, 51, v149
	v_cmp_gt_u32_e32 vcc, s2, v34
	v_cmp_gt_u32_e64 s[4:5], s2, v35
	v_cmp_gt_u32_e64 s[6:7], s2, v36
	v_cmp_gt_u32_e64 s[12:13], s2, v37
	v_cndmask_b32_e32 v106, v33, v106, vcc
	v_cndmask_b32_e64 v107, v33, v107, s[4:5]
	v_cndmask_b32_e64 v104, v33, v104, s[6:7]
	v_cndmask_b32_e64 v105, v33, v105, s[12:13]
	v_add_u32_e32 v34, 56, v149
	v_add_u32_e32 v35, 57, v149
	v_add_u32_e32 v36, 58, v149
	v_add_u32_e32 v37, 59, v149
	v_cmp_gt_u32_e32 vcc, s2, v34
	v_cmp_gt_u32_e64 s[4:5], s2, v35
	v_cmp_gt_u32_e64 s[6:7], s2, v36
	v_cmp_gt_u32_e64 s[12:13], s2, v37
	v_cndmask_b32_e32 v108, v33, v108, vcc
	v_cndmask_b32_e64 v109, v33, v109, s[4:5]
	v_cndmask_b32_e64 v110, v33, v110, s[6:7]
	v_cndmask_b32_e64 v111, v33, v111, s[12:13]
	v_max3_f32 v32, v96, s14, v97
	v_max3_f32 v32, v32, v98, v99
	v_max3_f32 v32, v32, v100, v101
	v_max3_f32 v32, v32, v102, v103
	v_max3_f32 v32, v32, v106, v107
	v_max3_f32 v32, v32, v104, v105
	v_max3_f32 v32, v32, v108, v109
	v_max3_f32 v148, v32, v110, v111
